# P9/P12 start stagger narrowed (sleep steps 2 and 3 instead of 3 and 4)
# baseline (speedup 1.0000x reference)
.LBB0_1169:
.LBB0_1170:
	s_cmp_lt_i32 s26, 32
	s_cbranch_scc1 .Lstag9_done
	s_and_b32 s98, s26, 3
	s_mul_i32 s98, s98, 2
	s_cmp_eq_u32 s98, 0
	s_cbranch_scc1 .Lstag9_done
